# combo5 + nt on P10 s[6:7]-based LDS-DMA loads (16 loads)
# baseline (speedup 1.0000x reference)
.LBB0_1468:
	s_or_b64 exec, exec, s[2:3]
	s_add_i32 s2, 0, 0x20200
	v_mov_b32_e32 v0, s2
	s_waitcnt lgkmcnt(0)
	s_barrier
	ds_read_b32 v0, v0
	s_movk_i32 s2, 0x200
	s_waitcnt lgkmcnt(0)
	v_lshlrev_b32_e32 v168, 3, v0
	v_cmp_ge_i32_e32 vcc, s0, v168
	v_readfirstlane_b32 s16, v0
	v_readfirstlane_b32 s17, v12
	s_cbranch_vccnz .LBB0_1491
	v_bfe_i32 v2, v12, 27, 1
	v_lshlrev_b32_e32 v1, 4, v12
	v_lshrrev_b32_e32 v2, 22, v2
	v_add_u32_e32 v2, v1, v2
	v_and_b32_e32 v2, 0xfffffc00, v2
	v_sub_u32_e32 v2, v1, v2
	v_ashrrev_i32_e32 v0, 31, v12
	v_lshrrev_b32_e32 v3, 4, v2
	v_lshrrev_b32_e32 v0, 26, v0
	v_bitop3_b32 v2, v3, v2, 32 bitop3:0x6c
	v_add_u32_e32 v0, v12, v0
	v_ashrrev_i32_e32 v4, 31, v2
	v_ashrrev_i32_e32 v0, 6, v0
	v_lshrrev_b32_e32 v4, 26, v4
	v_lshlrev_b32_e32 v3, 3, v0
	v_add_u32_e32 v4, v2, v4
	v_and_b32_e32 v3, -16, v3
	v_ashrrev_i32_e32 v5, 6, v4
	v_and_b32_e32 v4, 0xc0, v4
	v_add_u32_e32 v3, v5, v3
	v_sub_u32_e32 v2, v2, v4
	v_mov_b32_e32 v4, 1
	v_lshlrev_b32_e32 v0, 5, v0
	v_ashrrev_i16_sdwa v2, v4, sext(v2) dst_sel:DWORD dst_unused:UNUSED_PAD src0_sel:DWORD src1_sel:BYTE_0
	v_lshlrev_b32_e32 v6, 1, v3
	v_lshrrev_b32_e32 v7, 2, v3
	v_and_b32_e32 v5, 3, v5
	s_movk_i32 s3, 0xffe0
	v_and_b32_e32 v0, 32, v0
	v_bfe_i32 v2, v2, 0, 16
	v_and_b32_e32 v6, 24, v6
	v_and_b32_e32 v7, 4, v7
	v_and_or_b32 v5, v3, s3, v5
	v_or3_b32 v5, v5, v7, v6
	v_add_lshl_u32 v0, v0, v2, 1
	v_mad_u64_u32 v[16:17], s[6:7], v5, s2, v[0:1]
	v_add_u32_e32 v1, 0x2000, v1
	v_ashrrev_i32_e32 v2, 31, v1
	v_lshrrev_b32_e32 v2, 22, v2
	v_add_u32_e32 v2, v1, v2
	v_ashrrev_i32_e32 v2, 10, v2
	v_mul_i32_i24_e32 v5, 0x400, v2
	v_sub_u32_e32 v1, v1, v5
	v_lshrrev_b32_e32 v5, 4, v1
	v_bitop3_b32 v1, v5, v1, 32 bitop3:0x6c
	v_ashrrev_i32_e32 v6, 31, v1
	v_lshrrev_b32_e32 v6, 26, v6
	v_lshlrev_b32_e32 v5, 3, v2
	v_add_u32_e32 v6, v1, v6
	v_and_b32_e32 v5, -16, v5
	v_ashrrev_i32_e32 v7, 6, v6
	v_add_u32_e32 v5, v7, v5
	v_and_b32_e32 v7, 3, v7
	s_ashr_i32 s4, s17, 6
	v_and_or_b32 v7, v5, s3, v7
	s_ashr_i32 s3, s2, 31
	s_ashr_i32 s5, s17, 8
	s_lshl_b64 s[14:15], s[2:3], 7
	s_lshl_b32 s31, s4, 10
	s_add_u32 s33, s12, 0x40560200
	s_addc_u32 s54, s13, 0
	s_add_u32 s55, s12, 0x123b0200
	s_addc_u32 s56, s13, 0
	s_ashr_i32 s57, s0, 31
	s_lshr_b32 s6, s57, 29
	s_add_i32 s6, s0, s6
	s_ashr_i32 s7, s6, 3
	s_and_b32 s6, s6, -8
	s_sub_i32 s6, s0, s6
	s_add_i32 s58, s16, 1
	s_cmp_lt_i32 s6, 0
	s_cselect_b32 s8, s58, s16
	s_mul_i32 s6, s8, s6
	s_add_i32 s8, s6, s7
	s_ashr_i32 s6, s8, 31
	s_lshr_b32 s6, s6, 29
	v_and_b32_e32 v6, 0xc0, v6
	s_add_i32 s9, s8, s6
	v_sub_u32_e32 v1, v1, v6
	s_ashr_i32 s42, s9, 3
	v_lshlrev_b32_e32 v2, 5, v2
	v_ashrrev_i16_sdwa v1, v4, sext(v1) dst_sel:DWORD dst_unused:UNUSED_PAD src0_sel:DWORD src1_sel:BYTE_0
	s_add_i32 s6, s42, 0
	v_and_b32_e32 v2, 32, v2
	v_bfe_i32 v1, v1, 0, 16
	s_add_i32 s6, s6, 0x20000
	v_add_lshl_u32 v2, v2, v1, 1
	v_mov_b32_e32 v1, s6
	v_lshlrev_b32_e32 v4, 1, v5
	v_lshrrev_b32_e32 v6, 2, v5
	ds_read_u8 v1, v1
	v_and_b32_e32 v4, 24, v4
	v_and_b32_e32 v6, 4, v6
	v_or3_b32 v4, v7, v6, v4
	v_mad_u64_u32 v[170:171], s[6:7], v4, s2, v[2:3]
	s_and_b32 s6, s9, -8
	s_sub_i32 s44, s8, s6
	s_waitcnt lgkmcnt(0)
	v_readfirstlane_b32 s6, v1
	s_and_b32 s61, s6, 0xff
	s_lshl_b32 s6, s61, 20
	s_add_u32 s8, s55, s6
	s_addc_u32 s9, s56, 0
	s_ashr_i32 s45, s44, 31
	s_lshl_b64 s[6:7], s[44:45], 17
	s_add_u32 s48, s8, s6
	s_addc_u32 s49, s9, s7
	s_add_i32 s45, s31, 0
	s_add_i32 s59, s45, 0x10000
	s_ashr_i32 s43, s42, 31
	s_mov_b32 m0, s59
	s_add_i32 s60, s45, 0x12000
	s_lshl_b64 s[50:51], s[42:43], 17
	global_load_lds_dwordx4 v16, s[48:49]
	s_mov_b32 m0, s60
	s_add_u32 s6, s33, s50
	v_lshl_add_u32 v172, v3, 9, v0
	global_load_lds_dwordx4 v170, s[48:49]
	s_addc_u32 s7, s54, s51
	s_mov_b32 m0, s45
	s_add_i32 s43, s45, 0x2000
	v_lshl_add_u32 v176, v5, 9, v2
	global_load_lds_dwordx4 v172, s[6:7] nt
	s_mov_b32 m0, s43
	s_add_u32 s8, s48, s14
	global_load_lds_dwordx4 v176, s[6:7] nt
	s_addc_u32 s9, s49, s15
	s_add_i32 m0, s45, 0x14000
	s_add_i32 s62, s45, 0x4000
	global_load_lds_dwordx4 v16, s[8:9]
	s_add_i32 m0, s45, 0x16000
	v_add_u32_e32 v174, 0x10000, v172
	global_load_lds_dwordx4 v170, s[8:9]
	s_mov_b32 m0, s62
	s_add_i32 s63, s45, 0x6000
	v_add_u32_e32 v178, 0x10000, v176
	global_load_lds_dwordx4 v174, s[6:7] nt
	s_mov_b32 m0, s63
	v_mov_b32_e32 v181, 0
	global_load_lds_dwordx4 v178, s[6:7] nt
	v_mov_b32_e32 v17, v181
	v_mov_b32_e32 v171, v181
	v_mov_b32_e32 v173, v181
	v_mov_b32_e32 v177, v181
	v_lshl_add_u64 v[10:11], s[48:49], 0, v[16:17]
	v_lshl_add_u64 v[8:9], s[48:49], 0, v[170:171]
	v_lshl_add_u64 v[6:7], s[6:7], 0, v[172:173]
	v_lshl_add_u64 v[4:5], s[6:7], 0, v[176:177]
	v_lshl_add_u64 v[2:3], s[8:9], 0, v[16:17]
	s_cmp_lg_u32 s5, 1
	v_lshl_add_u64 v[0:1], s[8:9], 0, v[170:171]
	s_cbranch_scc1 .LBB0_1471
	s_barrier

.LBB0_1485:
	s_add_u32 s10, s50, 0xbfa9fe80
	s_addc_u32 s11, s51, -1
	s_add_i32 s73, 0, 0x10000
	v_add_u32_e32 v16, s73, v188
	ds_read_b128 v[30:33], v16
	ds_read_b128 v[34:37], v16 offset:1024
	ds_read_b128 v[38:41], v16 offset:2048
	ds_read_b128 v[42:45], v16 offset:3072
	s_cmp_eq_u32 s64, s53
	s_cselect_b32 s7, s41, s49
	s_cselect_b32 s6, s40, s48
	s_cselect_b32 s74, s39, s11
	s_cselect_b32 s75, s38, s10
	s_add_u32 s10, s12, s50
	s_addc_u32 s11, s13, s51
	s_add_i32 m0, s45, 0xc000
	ds_read_b128 v[20:23], v190
	ds_read_b128 v[24:27], v190 offset:1024
	ds_read_b128 v[46:49], v190 offset:2048
	ds_read_b128 v[50:53], v190 offset:3072
	ds_read_b128 v[192:195], v190 offset:4096
	ds_read_b128 v[196:199], v190 offset:5120
	ds_read_b128 v[200:203], v190 offset:6144
	ds_read_b128 v[204:207], v190 offset:7168
	global_load_lds_dwordx4 v174, s[10:11]
	s_add_i32 m0, s45, 0xe000
	s_nop 0
	global_load_lds_dwordx4 v178, s[10:11]
	s_waitcnt lgkmcnt(8)
	s_barrier
	s_waitcnt lgkmcnt(0)
	s_setprio 1
	s_waitcnt lgkmcnt(0)
	v_mfma_scale_f32_16x16x128_f8f6f4 v[136:139], v[30:37], v[20:27], v[136:139], v191, v191 op_sel_hi:[0,0,0]
	v_mfma_scale_f32_16x16x128_f8f6f4 v[140:143], v[38:45], v[20:27], v[140:143], v191, v191 op_sel_hi:[0,0,0]
	v_mfma_scale_f32_16x16x128_f8f6f4 v[120:123], v[30:37], v[46:53], v[120:123], v191, v191 op_sel_hi:[0,0,0]
	v_mfma_scale_f32_16x16x128_f8f6f4 v[124:127], v[38:45], v[46:53], v[124:127], v191, v191 op_sel_hi:[0,0,0]
	v_mfma_scale_f32_16x16x128_f8f6f4 v[96:99], v[30:37], v[192:199], v[96:99], v191, v191 op_sel_hi:[0,0,0]
	v_mfma_scale_f32_16x16x128_f8f6f4 v[100:103], v[38:45], v[192:199], v[100:103], v191, v191 op_sel_hi:[0,0,0]
	v_mfma_scale_f32_16x16x128_f8f6f4 v[80:83], v[30:37], v[200:207], v[80:83], v191, v191 op_sel_hi:[0,0,0]
	v_mfma_scale_f32_16x16x128_f8f6f4 v[84:87], v[38:45], v[200:207], v[84:87], v191, v191 op_sel_hi:[0,0,0]
	s_setprio 0
	s_barrier
	s_add_i32 s10, s73, s31
	s_mov_b32 m0, s10
	ds_read_b128 v[208:211], v175
	ds_read_b128 v[212:215], v175 offset:1024
	ds_read_b128 v[218:221], v175 offset:2048
	ds_read_b128 v[222:225], v175 offset:3072
	global_load_lds_dwordx4 v180, s[6:7] nt
	s_add_i32 m0, s10, 0x2000
	v_mov_b32_e32 v171, v181
	global_load_lds_dwordx4 v170, s[6:7] nt
	s_barrier
	s_waitcnt lgkmcnt(0)
	v_lshl_add_u64 v[18:19], s[6:7], 0, v[180:181]
	v_lshl_add_u64 v[16:17], s[6:7], 0, v[170:171]
	s_setprio 1
	s_waitcnt lgkmcnt(0)
	v_mfma_scale_f32_16x16x128_f8f6f4 v[160:163], v[208:215], v[20:27], v[160:163], v191, v191 op_sel_hi:[0,0,0]
	v_mfma_scale_f32_16x16x128_f8f6f4 v[164:167], v[218:225], v[20:27], v[164:167], v191, v191 op_sel_hi:[0,0,0]
	v_mfma_scale_f32_16x16x128_f8f6f4 v[144:147], v[208:215], v[46:53], v[144:147], v191, v191 op_sel_hi:[0,0,0]
	v_mfma_scale_f32_16x16x128_f8f6f4 v[152:155], v[218:225], v[46:53], v[152:155], v191, v191 op_sel_hi:[0,0,0]
	v_mfma_scale_f32_16x16x128_f8f6f4 v[128:131], v[208:215], v[192:199], v[128:131], v191, v191 op_sel_hi:[0,0,0]
	v_mfma_scale_f32_16x16x128_f8f6f4 v[132:135], v[218:225], v[192:199], v[132:135], v191, v191 op_sel_hi:[0,0,0]
	v_mfma_scale_f32_16x16x128_f8f6f4 v[104:107], v[208:215], v[200:207], v[104:107], v191, v191 op_sel_hi:[0,0,0]
	v_mfma_scale_f32_16x16x128_f8f6f4 v[112:115], v[218:225], v[200:207], v[112:115], v191, v191 op_sel_hi:[0,0,0]
	s_setprio 0
	s_add_u32 s10, s33, s75
	s_mov_b32 m0, s45
	s_addc_u32 s11, s54, s74
	s_barrier
	ds_read_b128 v[46:49], v190 offset:16384
	ds_read_b128 v[50:53], v190 offset:17408
	ds_read_b128 v[192:195], v190 offset:18432
	ds_read_b128 v[196:199], v190 offset:19456
	ds_read_b128 v[200:203], v190 offset:20480
	ds_read_b128 v[204:207], v190 offset:21504
	ds_read_b128 v[226:229], v190 offset:22528
	ds_read_b128 v[230:233], v190 offset:23552
	global_load_lds_dwordx4 v172, s[10:11]
	s_mov_b32 m0, s43
	v_mov_b32_e32 v173, v181
	global_load_lds_dwordx4 v176, s[10:11]
	s_barrier
	s_waitcnt lgkmcnt(0)
	v_mov_b32_e32 v177, v181
	v_lshl_add_u64 v[26:27], s[10:11], 0, v[172:173]
	v_lshl_add_u64 v[22:23], s[10:11], 0, v[176:177]
	s_setprio 1
	s_waitcnt lgkmcnt(0)
	v_mfma_scale_f32_16x16x128_f8f6f4 v[108:111], v[30:37], v[46:53], v[108:111], v191, v191 op_sel_hi:[0,0,0]
	v_mfma_scale_f32_16x16x128_f8f6f4 v[116:119], v[38:45], v[46:53], v[116:119], v191, v191 op_sel_hi:[0,0,0]
	v_mfma_scale_f32_16x16x128_f8f6f4 v[88:91], v[30:37], v[192:199], v[88:91], v191, v191 op_sel_hi:[0,0,0]
	v_mfma_scale_f32_16x16x128_f8f6f4 v[92:95], v[38:45], v[192:199], v[92:95], v191, v191 op_sel_hi:[0,0,0]
	v_mfma_scale_f32_16x16x128_f8f6f4 v[72:75], v[30:37], v[200:207], v[72:75], v191, v191 op_sel_hi:[0,0,0]
	v_mfma_scale_f32_16x16x128_f8f6f4 v[76:79], v[38:45], v[200:207], v[76:79], v191, v191 op_sel_hi:[0,0,0]
	v_mfma_scale_f32_16x16x128_f8f6f4 v[68:71], v[30:37], v[226:233], v[68:71], v191, v191 op_sel_hi:[0,0,0]
	v_mfma_scale_f32_16x16x128_f8f6f4 v[64:67], v[38:45], v[226:233], v[64:67], v191, v191 op_sel_hi:[0,0,0]
	s_setprio 0
	s_barrier
	s_add_u32 s6, s6, s14
	s_mov_b32 m0, s35
	s_addc_u32 s7, s7, s15
	global_load_lds_dwordx4 v180, s[6:7] nt
	s_mov_b32 m0, s37
	v_lshl_add_u64 v[24:25], s[6:7], 0, v[180:181]
	global_load_lds_dwordx4 v170, s[6:7] nt
	s_waitcnt vmcnt(6)
	v_lshl_add_u64 v[20:21], s[6:7], 0, v[170:171]
	s_barrier
	s_setprio 1
	v_mfma_scale_f32_16x16x128_f8f6f4 v[148:151], v[208:215], v[46:53], v[148:151], v191, v191 op_sel_hi:[0,0,0]
	v_mfma_scale_f32_16x16x128_f8f6f4 v[156:159], v[218:225], v[46:53], v[156:159], v191, v191 op_sel_hi:[0,0,0]
	v_mfma_scale_f32_16x16x128_f8f6f4 v[56:59], v[208:215], v[192:199], v[56:59], v191, v191 op_sel_hi:[0,0,0]
	v_mfma_scale_f32_16x16x128_f8f6f4 v[60:63], v[218:225], v[192:199], v[60:63], v191, v191 op_sel_hi:[0,0,0]
	v_mfma_scale_f32_16x16x128_f8f6f4 v[8:11], v[208:215], v[200:207], v[8:11], v191, v191 op_sel_hi:[0,0,0]
	v_mfma_scale_f32_16x16x128_f8f6f4 v[12:15], v[218:225], v[200:207], v[12:15], v191, v191 op_sel_hi:[0,0,0]
	v_mfma_scale_f32_16x16x128_f8f6f4 v[4:7], v[208:215], v[226:233], v[4:7], v191, v191 op_sel_hi:[0,0,0]
	v_mfma_scale_f32_16x16x128_f8f6f4 v[0:3], v[218:225], v[226:233], v[0:3], v191, v191 op_sel_hi:[0,0,0]
	s_setprio 0
	s_barrier
	ds_read_b128 v[30:33], v28
	ds_read_b128 v[34:37], v28 offset:1024
	ds_read_b128 v[38:41], v28 offset:2048
	ds_read_b128 v[42:45], v28 offset:3072
	s_mov_b32 m0, s62
	ds_read_b128 v[46:49], v190 offset:32768
	ds_read_b128 v[50:53], v190 offset:33792
	ds_read_b128 v[192:195], v190 offset:34816
	ds_read_b128 v[196:199], v190 offset:35840
	ds_read_b128 v[200:203], v190 offset:36864
	ds_read_b128 v[204:207], v190 offset:37888
	ds_read_b128 v[208:211], v190 offset:38912
	ds_read_b128 v[212:215], v190 offset:39936
	global_load_lds_dwordx4 v174, s[10:11]
	s_mov_b32 m0, s63
	s_nop 0
	global_load_lds_dwordx4 v178, s[10:11]
	s_waitcnt lgkmcnt(8)
	s_barrier
	s_waitcnt lgkmcnt(0)
	s_setprio 1
	s_waitcnt lgkmcnt(0)
	v_mfma_scale_f32_16x16x128_f8f6f4 v[136:139], v[30:37], v[46:53], v[136:139], v191, v191 op_sel_hi:[0,0,0]
	v_mfma_scale_f32_16x16x128_f8f6f4 v[140:143], v[38:45], v[46:53], v[140:143], v191, v191 op_sel_hi:[0,0,0]
	v_mfma_scale_f32_16x16x128_f8f6f4 v[120:123], v[30:37], v[192:199], v[120:123], v191, v191 op_sel_hi:[0,0,0]
	v_mfma_scale_f32_16x16x128_f8f6f4 v[124:127], v[38:45], v[192:199], v[124:127], v191, v191 op_sel_hi:[0,0,0]
	v_mfma_scale_f32_16x16x128_f8f6f4 v[96:99], v[30:37], v[200:207], v[96:99], v191, v191 op_sel_hi:[0,0,0]
	v_mfma_scale_f32_16x16x128_f8f6f4 v[100:103], v[38:45], v[200:207], v[100:103], v191, v191 op_sel_hi:[0,0,0]
	v_mfma_scale_f32_16x16x128_f8f6f4 v[80:83], v[30:37], v[208:215], v[80:83], v191, v191 op_sel_hi:[0,0,0]
	v_mfma_scale_f32_16x16x128_f8f6f4 v[84:87], v[38:45], v[208:215], v[84:87], v191, v191 op_sel_hi:[0,0,0]
	s_setprio 0
	s_barrier
	s_mov_b32 m0, s9
	v_lshl_add_u64 v[18:19], v[18:19], 0, s[22:23]
	ds_read_b128 v[218:221], v29
	ds_read_b128 v[222:225], v29 offset:1024
	ds_read_b128 v[226:229], v29 offset:2048
	ds_read_b128 v[230:233], v29 offset:3072
	global_load_lds_dwordx4 v[18:19], off
	v_lshl_add_u64 v[16:17], v[16:17], 0, s[22:23]
	s_mov_b32 m0, s28
	s_nop 0
	global_load_lds_dwordx4 v[16:17], off
	s_barrier
	s_waitcnt lgkmcnt(0)
	s_setprio 1
	s_waitcnt lgkmcnt(0)
	v_mfma_scale_f32_16x16x128_f8f6f4 v[160:163], v[218:225], v[46:53], v[160:163], v191, v191 op_sel_hi:[0,0,0]
	v_mfma_scale_f32_16x16x128_f8f6f4 v[164:167], v[226:233], v[46:53], v[164:167], v191, v191 op_sel_hi:[0,0,0]
	v_mfma_scale_f32_16x16x128_f8f6f4 v[144:147], v[218:225], v[192:199], v[144:147], v191, v191 op_sel_hi:[0,0,0]
	v_mfma_scale_f32_16x16x128_f8f6f4 v[152:155], v[226:233], v[192:199], v[152:155], v191, v191 op_sel_hi:[0,0,0]
	v_mfma_scale_f32_16x16x128_f8f6f4 v[128:131], v[218:225], v[200:207], v[128:131], v191, v191 op_sel_hi:[0,0,0]
	v_mfma_scale_f32_16x16x128_f8f6f4 v[132:135], v[226:233], v[200:207], v[132:135], v191, v191 op_sel_hi:[0,0,0]
	v_mfma_scale_f32_16x16x128_f8f6f4 v[104:107], v[218:225], v[208:215], v[104:107], v191, v191 op_sel_hi:[0,0,0]
	v_mfma_scale_f32_16x16x128_f8f6f4 v[112:115], v[226:233], v[208:215], v[112:115], v191, v191 op_sel_hi:[0,0,0]
	s_setprio 0
	s_mov_b32 m0, s66
	v_lshl_add_u64 v[16:17], v[26:27], 0, s[22:23]
	s_barrier
	ds_read_b128 v[46:49], v190 offset:49152
	ds_read_b128 v[50:53], v190 offset:50176
	ds_read_b128 v[192:195], v190 offset:51200
	ds_read_b128 v[196:199], v190 offset:52224
	ds_read_b128 v[200:203], v190 offset:53248
	ds_read_b128 v[204:207], v190 offset:54272
	ds_read_b128 v[208:211], v190 offset:55296
	ds_read_b128 v[212:215], v190 offset:56320
	global_load_lds_dwordx4 v[16:17], off
	v_lshl_add_u64 v[16:17], v[22:23], 0, s[22:23]
	s_mov_b32 m0, s67
	s_nop 0
	global_load_lds_dwordx4 v[16:17], off
	s_barrier
	s_waitcnt lgkmcnt(0)
	s_setprio 1
	s_waitcnt lgkmcnt(0)
	v_mfma_scale_f32_16x16x128_f8f6f4 v[108:111], v[30:37], v[46:53], v[108:111], v191, v191 op_sel_hi:[0,0,0]
	v_mfma_scale_f32_16x16x128_f8f6f4 v[116:119], v[38:45], v[46:53], v[116:119], v191, v191 op_sel_hi:[0,0,0]
	v_mfma_scale_f32_16x16x128_f8f6f4 v[88:91], v[30:37], v[192:199], v[88:91], v191, v191 op_sel_hi:[0,0,0]
	v_mfma_scale_f32_16x16x128_f8f6f4 v[92:95], v[38:45], v[192:199], v[92:95], v191, v191 op_sel_hi:[0,0,0]
	v_mfma_scale_f32_16x16x128_f8f6f4 v[72:75], v[30:37], v[200:207], v[72:75], v191, v191 op_sel_hi:[0,0,0]
	v_mfma_scale_f32_16x16x128_f8f6f4 v[76:79], v[38:45], v[200:207], v[76:79], v191, v191 op_sel_hi:[0,0,0]
	v_mfma_scale_f32_16x16x128_f8f6f4 v[68:71], v[30:37], v[208:215], v[68:71], v191, v191 op_sel_hi:[0,0,0]
	v_mfma_scale_f32_16x16x128_f8f6f4 v[64:67], v[38:45], v[208:215], v[64:67], v191, v191 op_sel_hi:[0,0,0]
	s_setprio 0
	s_barrier
	s_mov_b32 m0, s29
	v_lshl_add_u64 v[16:17], v[24:25], 0, s[22:23]
	global_load_lds_dwordx4 v[16:17], off
	v_lshl_add_u64 v[16:17], v[20:21], 0, s[22:23]
	s_mov_b32 m0, s52
	s_nop 0
	global_load_lds_dwordx4 v[16:17], off
	s_waitcnt vmcnt(6)
	s_barrier
	s_setprio 1
	v_mfma_scale_f32_16x16x128_f8f6f4 v[148:151], v[218:225], v[46:53], v[148:151], v191, v191 op_sel_hi:[0,0,0]
	v_mfma_scale_f32_16x16x128_f8f6f4 v[156:159], v[226:233], v[46:53], v[156:159], v191, v191 op_sel_hi:[0,0,0]
	v_mfma_scale_f32_16x16x128_f8f6f4 v[56:59], v[218:225], v[192:199], v[56:59], v191, v191 op_sel_hi:[0,0,0]
	v_mfma_scale_f32_16x16x128_f8f6f4 v[60:63], v[226:233], v[192:199], v[60:63], v191, v191 op_sel_hi:[0,0,0]
	v_mfma_scale_f32_16x16x128_f8f6f4 v[8:11], v[218:225], v[200:207], v[8:11], v191, v191 op_sel_hi:[0,0,0]
	v_mfma_scale_f32_16x16x128_f8f6f4 v[12:15], v[226:233], v[200:207], v[12:15], v191, v191 op_sel_hi:[0,0,0]
	v_mfma_scale_f32_16x16x128_f8f6f4 v[4:7], v[218:225], v[208:215], v[4:7], v191, v191 op_sel_hi:[0,0,0]
	v_mfma_scale_f32_16x16x128_f8f6f4 v[0:3], v[226:233], v[208:215], v[0:3], v191, v191 op_sel_hi:[0,0,0]
	s_setprio 0
	s_add_u32 s50, s50, 0x100
	s_addc_u32 s51, s51, 0
	s_add_i32 s6, s53, 2
	s_add_u32 s48, s48, 0x100
	s_addc_u32 s49, s49, 0
	s_cmp_ge_i32 s53, s64
	s_mov_b32 s53, s6
	s_barrier
	s_cbranch_scc0 .LBB0_1485

.LBB0_2745:
	s_or_b64 exec, exec, s[2:3]
	s_add_i32 s2, 0, 0x20200
	v_mov_b32_e32 v0, s2
	s_waitcnt lgkmcnt(0)
	s_barrier
	ds_read_b32 v0, v0
	s_movk_i32 s2, 0x200
	s_waitcnt lgkmcnt(0)
	v_lshlrev_b32_e32 v168, 3, v0
	v_cmp_ge_i32_e32 vcc, s1, v168
	v_readfirstlane_b32 s16, v0
	v_readfirstlane_b32 s17, v12
	s_cbranch_vccnz .LBB0_2768
	v_bfe_i32 v2, v12, 27, 1
	v_lshlrev_b32_e32 v1, 4, v12
	v_lshrrev_b32_e32 v2, 22, v2
	v_add_u32_e32 v2, v1, v2
	v_and_b32_e32 v2, 0xfffffc00, v2
	v_sub_u32_e32 v2, v1, v2
	v_ashrrev_i32_e32 v0, 31, v12
	v_lshrrev_b32_e32 v3, 4, v2
	v_lshrrev_b32_e32 v0, 26, v0
	v_bitop3_b32 v2, v3, v2, 32 bitop3:0x6c
	v_add_u32_e32 v0, v12, v0
	v_ashrrev_i32_e32 v4, 31, v2
	v_ashrrev_i32_e32 v0, 6, v0
	v_lshrrev_b32_e32 v4, 26, v4
	v_lshlrev_b32_e32 v3, 3, v0
	v_add_u32_e32 v4, v2, v4
	v_and_b32_e32 v3, -16, v3
	v_ashrrev_i32_e32 v5, 6, v4
	v_and_b32_e32 v4, 0xc0, v4
	v_add_u32_e32 v3, v5, v3
	v_sub_u32_e32 v2, v2, v4
	v_mov_b32_e32 v4, 1
	v_lshlrev_b32_e32 v0, 5, v0
	v_ashrrev_i16_sdwa v2, v4, sext(v2) dst_sel:DWORD dst_unused:UNUSED_PAD src0_sel:DWORD src1_sel:BYTE_0
	v_lshlrev_b32_e32 v6, 1, v3
	v_lshrrev_b32_e32 v7, 2, v3
	v_and_b32_e32 v5, 3, v5
	s_movk_i32 s3, 0xffe0
	v_and_b32_e32 v0, 32, v0
	v_bfe_i32 v2, v2, 0, 16
	v_and_b32_e32 v6, 24, v6
	v_and_b32_e32 v7, 4, v7
	v_and_or_b32 v5, v3, s3, v5
	v_or3_b32 v5, v5, v7, v6
	v_add_lshl_u32 v0, v0, v2, 1
	v_mad_u64_u32 v[16:17], s[6:7], v5, s2, v[0:1]
	v_add_u32_e32 v1, 0x2000, v1
	v_ashrrev_i32_e32 v2, 31, v1
	v_lshrrev_b32_e32 v2, 22, v2
	v_add_u32_e32 v2, v1, v2
	v_ashrrev_i32_e32 v2, 10, v2
	v_mul_i32_i24_e32 v5, 0x400, v2
	v_sub_u32_e32 v1, v1, v5
	v_lshrrev_b32_e32 v5, 4, v1
	v_bitop3_b32 v1, v5, v1, 32 bitop3:0x6c
	v_ashrrev_i32_e32 v6, 31, v1
	v_lshrrev_b32_e32 v6, 26, v6
	v_lshlrev_b32_e32 v5, 3, v2
	v_add_u32_e32 v6, v1, v6
	v_and_b32_e32 v5, -16, v5
	v_ashrrev_i32_e32 v7, 6, v6
	v_add_u32_e32 v5, v7, v5
	v_and_b32_e32 v7, 3, v7
	s_ashr_i32 s4, s17, 6
	v_and_or_b32 v7, v5, s3, v7
	s_ashr_i32 s3, s2, 31
	s_ashr_i32 s5, s17, 8
	s_lshl_b64 s[14:15], s[2:3], 7
	s_lshl_b32 s31, s4, 10
	s_add_u32 s33, s12, 0x40560200
	s_addc_u32 s54, s13, 0
	s_add_u32 s55, s12, 0x2c360200
	s_addc_u32 s56, s13, 0
	s_ashr_i32 s57, s1, 31
	s_lshr_b32 s6, s57, 29
	s_add_i32 s6, s1, s6
	s_ashr_i32 s7, s6, 3
	s_and_b32 s6, s6, -8
	s_sub_i32 s6, s1, s6
	s_add_i32 s58, s16, 1
	s_cmp_lt_i32 s6, 0
	s_cselect_b32 s8, s58, s16
	s_mul_i32 s6, s8, s6
	s_add_i32 s8, s6, s7
	s_ashr_i32 s6, s8, 31
	s_lshr_b32 s6, s6, 29
	v_and_b32_e32 v6, 0xc0, v6
	s_add_i32 s9, s8, s6
	v_sub_u32_e32 v1, v1, v6
	s_ashr_i32 s42, s9, 3
	v_lshlrev_b32_e32 v2, 5, v2
	v_ashrrev_i16_sdwa v1, v4, sext(v1) dst_sel:DWORD dst_unused:UNUSED_PAD src0_sel:DWORD src1_sel:BYTE_0
	s_add_i32 s6, s42, 0
	v_and_b32_e32 v2, 32, v2
	v_bfe_i32 v1, v1, 0, 16
	s_add_i32 s6, s6, 0x20000
	v_add_lshl_u32 v2, v2, v1, 1
	v_mov_b32_e32 v1, s6
	v_lshlrev_b32_e32 v4, 1, v5
	v_lshrrev_b32_e32 v6, 2, v5
	ds_read_u8 v1, v1
	v_and_b32_e32 v4, 24, v4
	v_and_b32_e32 v6, 4, v6
	v_or3_b32 v4, v7, v6, v4
	v_mad_u64_u32 v[170:171], s[6:7], v4, s2, v[2:3]
	s_and_b32 s6, s9, -8
	s_sub_i32 s44, s8, s6
	s_waitcnt lgkmcnt(0)
	v_readfirstlane_b32 s6, v1
	s_and_b32 s61, s6, 0xff
	s_lshl_b32 s6, s61, 20
	s_add_u32 s8, s55, s6
	s_addc_u32 s9, s56, 0
	s_ashr_i32 s45, s44, 31
	s_lshl_b64 s[6:7], s[44:45], 17
	s_add_u32 s48, s8, s6
	s_addc_u32 s49, s9, s7
	s_add_i32 s45, s31, 0
	s_add_i32 s59, s45, 0x10000
	s_ashr_i32 s43, s42, 31
	s_mov_b32 m0, s59
	s_add_i32 s60, s45, 0x12000
	s_lshl_b64 s[50:51], s[42:43], 17
	global_load_lds_dwordx4 v16, s[48:49]
	s_mov_b32 m0, s60
	s_add_u32 s6, s33, s50
	v_lshl_add_u32 v172, v3, 9, v0
	global_load_lds_dwordx4 v170, s[48:49]
	s_addc_u32 s7, s54, s51
	s_mov_b32 m0, s45
	s_add_i32 s43, s45, 0x2000
	v_lshl_add_u32 v176, v5, 9, v2
	global_load_lds_dwordx4 v172, s[6:7] nt
	s_mov_b32 m0, s43
	s_add_u32 s8, s48, s14
	global_load_lds_dwordx4 v176, s[6:7] nt
	s_addc_u32 s9, s49, s15
	s_add_i32 m0, s45, 0x14000
	s_add_i32 s62, s45, 0x4000
	global_load_lds_dwordx4 v16, s[8:9]
	s_add_i32 m0, s45, 0x16000
	v_add_u32_e32 v174, 0x10000, v172
	global_load_lds_dwordx4 v170, s[8:9]
	s_mov_b32 m0, s62
	s_add_i32 s63, s45, 0x6000
	v_add_u32_e32 v178, 0x10000, v176
	global_load_lds_dwordx4 v174, s[6:7] nt
	s_mov_b32 m0, s63
	v_mov_b32_e32 v181, 0
	global_load_lds_dwordx4 v178, s[6:7] nt
	v_mov_b32_e32 v17, v181
	v_mov_b32_e32 v171, v181
	v_mov_b32_e32 v173, v181
	v_mov_b32_e32 v177, v181
	v_lshl_add_u64 v[10:11], s[48:49], 0, v[16:17]
	v_lshl_add_u64 v[8:9], s[48:49], 0, v[170:171]
	v_lshl_add_u64 v[6:7], s[6:7], 0, v[172:173]
	v_lshl_add_u64 v[4:5], s[6:7], 0, v[176:177]
	v_lshl_add_u64 v[2:3], s[8:9], 0, v[16:17]
	s_cmp_lg_u32 s5, 1
	v_lshl_add_u64 v[0:1], s[8:9], 0, v[170:171]
	s_cbranch_scc1 .LBB0_2748
	s_barrier

.LBB0_2762:
	s_add_u32 s10, s50, 0xbfa9fe80
	s_addc_u32 s11, s51, -1
	s_add_i32 s73, 0, 0x10000
	v_add_u32_e32 v16, s73, v188
	ds_read_b128 v[30:33], v16
	ds_read_b128 v[34:37], v16 offset:1024
	ds_read_b128 v[38:41], v16 offset:2048
	ds_read_b128 v[42:45], v16 offset:3072
	s_cmp_eq_u32 s64, s53
	s_cselect_b32 s7, s41, s49
	s_cselect_b32 s6, s40, s48
	s_cselect_b32 s74, s39, s11
	s_cselect_b32 s75, s38, s10
	s_add_u32 s10, s12, s50
	s_addc_u32 s11, s13, s51
	s_add_i32 m0, s45, 0xc000
	ds_read_b128 v[20:23], v190
	ds_read_b128 v[24:27], v190 offset:1024
	ds_read_b128 v[46:49], v190 offset:2048
	ds_read_b128 v[50:53], v190 offset:3072
	ds_read_b128 v[192:195], v190 offset:4096
	ds_read_b128 v[196:199], v190 offset:5120
	ds_read_b128 v[200:203], v190 offset:6144
	ds_read_b128 v[204:207], v190 offset:7168
	global_load_lds_dwordx4 v174, s[10:11]
	s_add_i32 m0, s45, 0xe000
	s_nop 0
	global_load_lds_dwordx4 v178, s[10:11]
	s_waitcnt lgkmcnt(8)
	s_barrier
	s_waitcnt lgkmcnt(0)
	s_setprio 1
	s_waitcnt lgkmcnt(0)
	v_mfma_scale_f32_16x16x128_f8f6f4 v[136:139], v[30:37], v[20:27], v[136:139], v191, v191 op_sel_hi:[0,0,0]
	v_mfma_scale_f32_16x16x128_f8f6f4 v[140:143], v[38:45], v[20:27], v[140:143], v191, v191 op_sel_hi:[0,0,0]
	v_mfma_scale_f32_16x16x128_f8f6f4 v[120:123], v[30:37], v[46:53], v[120:123], v191, v191 op_sel_hi:[0,0,0]
	v_mfma_scale_f32_16x16x128_f8f6f4 v[124:127], v[38:45], v[46:53], v[124:127], v191, v191 op_sel_hi:[0,0,0]
	v_mfma_scale_f32_16x16x128_f8f6f4 v[96:99], v[30:37], v[192:199], v[96:99], v191, v191 op_sel_hi:[0,0,0]
	v_mfma_scale_f32_16x16x128_f8f6f4 v[100:103], v[38:45], v[192:199], v[100:103], v191, v191 op_sel_hi:[0,0,0]
	v_mfma_scale_f32_16x16x128_f8f6f4 v[80:83], v[30:37], v[200:207], v[80:83], v191, v191 op_sel_hi:[0,0,0]
	v_mfma_scale_f32_16x16x128_f8f6f4 v[84:87], v[38:45], v[200:207], v[84:87], v191, v191 op_sel_hi:[0,0,0]
	s_setprio 0
	s_barrier
	s_add_i32 s10, s73, s31
	s_mov_b32 m0, s10
	ds_read_b128 v[208:211], v175
	ds_read_b128 v[212:215], v175 offset:1024
	ds_read_b128 v[216:219], v175 offset:2048
	ds_read_b128 v[220:223], v175 offset:3072
	global_load_lds_dwordx4 v180, s[6:7] nt
	s_add_i32 m0, s10, 0x2000
	v_mov_b32_e32 v171, v181
	global_load_lds_dwordx4 v170, s[6:7] nt
	s_barrier
	s_waitcnt lgkmcnt(0)
	v_lshl_add_u64 v[18:19], s[6:7], 0, v[180:181]
	v_lshl_add_u64 v[16:17], s[6:7], 0, v[170:171]
	s_setprio 1
	s_waitcnt lgkmcnt(0)
	v_mfma_scale_f32_16x16x128_f8f6f4 v[160:163], v[208:215], v[20:27], v[160:163], v191, v191 op_sel_hi:[0,0,0]
	v_mfma_scale_f32_16x16x128_f8f6f4 v[164:167], v[216:223], v[20:27], v[164:167], v191, v191 op_sel_hi:[0,0,0]
	v_mfma_scale_f32_16x16x128_f8f6f4 v[144:147], v[208:215], v[46:53], v[144:147], v191, v191 op_sel_hi:[0,0,0]
	v_mfma_scale_f32_16x16x128_f8f6f4 v[152:155], v[216:223], v[46:53], v[152:155], v191, v191 op_sel_hi:[0,0,0]
	v_mfma_scale_f32_16x16x128_f8f6f4 v[128:131], v[208:215], v[192:199], v[128:131], v191, v191 op_sel_hi:[0,0,0]
	v_mfma_scale_f32_16x16x128_f8f6f4 v[132:135], v[216:223], v[192:199], v[132:135], v191, v191 op_sel_hi:[0,0,0]
	v_mfma_scale_f32_16x16x128_f8f6f4 v[104:107], v[208:215], v[200:207], v[104:107], v191, v191 op_sel_hi:[0,0,0]
	v_mfma_scale_f32_16x16x128_f8f6f4 v[112:115], v[216:223], v[200:207], v[112:115], v191, v191 op_sel_hi:[0,0,0]
	s_setprio 0
	s_add_u32 s10, s33, s75
	s_mov_b32 m0, s45
	s_addc_u32 s11, s54, s74
	s_barrier
	ds_read_b128 v[46:49], v190 offset:16384
	ds_read_b128 v[50:53], v190 offset:17408
	ds_read_b128 v[192:195], v190 offset:18432
	ds_read_b128 v[196:199], v190 offset:19456
	ds_read_b128 v[200:203], v190 offset:20480
	ds_read_b128 v[204:207], v190 offset:21504
	ds_read_b128 v[224:227], v190 offset:22528
	ds_read_b128 v[228:231], v190 offset:23552
	global_load_lds_dwordx4 v172, s[10:11]
	s_mov_b32 m0, s43
	v_mov_b32_e32 v173, v181
	global_load_lds_dwordx4 v176, s[10:11]
	s_barrier
	s_waitcnt lgkmcnt(0)
	v_mov_b32_e32 v177, v181
	v_lshl_add_u64 v[26:27], s[10:11], 0, v[172:173]
	v_lshl_add_u64 v[22:23], s[10:11], 0, v[176:177]
	s_setprio 1
	s_waitcnt lgkmcnt(0)
	v_mfma_scale_f32_16x16x128_f8f6f4 v[108:111], v[30:37], v[46:53], v[108:111], v191, v191 op_sel_hi:[0,0,0]
	v_mfma_scale_f32_16x16x128_f8f6f4 v[116:119], v[38:45], v[46:53], v[116:119], v191, v191 op_sel_hi:[0,0,0]
	v_mfma_scale_f32_16x16x128_f8f6f4 v[88:91], v[30:37], v[192:199], v[88:91], v191, v191 op_sel_hi:[0,0,0]
	v_mfma_scale_f32_16x16x128_f8f6f4 v[92:95], v[38:45], v[192:199], v[92:95], v191, v191 op_sel_hi:[0,0,0]
	v_mfma_scale_f32_16x16x128_f8f6f4 v[72:75], v[30:37], v[200:207], v[72:75], v191, v191 op_sel_hi:[0,0,0]
	v_mfma_scale_f32_16x16x128_f8f6f4 v[76:79], v[38:45], v[200:207], v[76:79], v191, v191 op_sel_hi:[0,0,0]
	v_mfma_scale_f32_16x16x128_f8f6f4 v[68:71], v[30:37], v[224:231], v[68:71], v191, v191 op_sel_hi:[0,0,0]
	v_mfma_scale_f32_16x16x128_f8f6f4 v[64:67], v[38:45], v[224:231], v[64:67], v191, v191 op_sel_hi:[0,0,0]
	s_setprio 0
	s_barrier
	s_add_u32 s6, s6, s14
	s_mov_b32 m0, s35
	s_addc_u32 s7, s7, s15
	global_load_lds_dwordx4 v180, s[6:7] nt
	s_mov_b32 m0, s37
	v_lshl_add_u64 v[24:25], s[6:7], 0, v[180:181]
	global_load_lds_dwordx4 v170, s[6:7] nt
	s_waitcnt vmcnt(6)
	v_lshl_add_u64 v[20:21], s[6:7], 0, v[170:171]
	s_barrier
	s_setprio 1
	v_mfma_scale_f32_16x16x128_f8f6f4 v[148:151], v[208:215], v[46:53], v[148:151], v191, v191 op_sel_hi:[0,0,0]
	v_mfma_scale_f32_16x16x128_f8f6f4 v[156:159], v[216:223], v[46:53], v[156:159], v191, v191 op_sel_hi:[0,0,0]
	v_mfma_scale_f32_16x16x128_f8f6f4 v[56:59], v[208:215], v[192:199], v[56:59], v191, v191 op_sel_hi:[0,0,0]
	v_mfma_scale_f32_16x16x128_f8f6f4 v[60:63], v[216:223], v[192:199], v[60:63], v191, v191 op_sel_hi:[0,0,0]
	v_mfma_scale_f32_16x16x128_f8f6f4 v[8:11], v[208:215], v[200:207], v[8:11], v191, v191 op_sel_hi:[0,0,0]
	v_mfma_scale_f32_16x16x128_f8f6f4 v[12:15], v[216:223], v[200:207], v[12:15], v191, v191 op_sel_hi:[0,0,0]
	v_mfma_scale_f32_16x16x128_f8f6f4 v[4:7], v[208:215], v[224:231], v[4:7], v191, v191 op_sel_hi:[0,0,0]
	v_mfma_scale_f32_16x16x128_f8f6f4 v[0:3], v[216:223], v[224:231], v[0:3], v191, v191 op_sel_hi:[0,0,0]
	s_setprio 0
	s_barrier
	ds_read_b128 v[30:33], v28
	ds_read_b128 v[34:37], v28 offset:1024
	ds_read_b128 v[38:41], v28 offset:2048
	ds_read_b128 v[42:45], v28 offset:3072
	s_mov_b32 m0, s62
	ds_read_b128 v[46:49], v190 offset:32768
	ds_read_b128 v[50:53], v190 offset:33792
	ds_read_b128 v[192:195], v190 offset:34816
	ds_read_b128 v[196:199], v190 offset:35840
	ds_read_b128 v[200:203], v190 offset:36864
	ds_read_b128 v[204:207], v190 offset:37888
	ds_read_b128 v[208:211], v190 offset:38912
	ds_read_b128 v[212:215], v190 offset:39936
	global_load_lds_dwordx4 v174, s[10:11]
	s_mov_b32 m0, s63
	s_nop 0
	global_load_lds_dwordx4 v178, s[10:11]
	s_waitcnt lgkmcnt(8)
	s_barrier
	s_waitcnt lgkmcnt(0)
	s_setprio 1
	s_waitcnt lgkmcnt(0)
	v_mfma_scale_f32_16x16x128_f8f6f4 v[136:139], v[30:37], v[46:53], v[136:139], v191, v191 op_sel_hi:[0,0,0]
	v_mfma_scale_f32_16x16x128_f8f6f4 v[140:143], v[38:45], v[46:53], v[140:143], v191, v191 op_sel_hi:[0,0,0]
	v_mfma_scale_f32_16x16x128_f8f6f4 v[120:123], v[30:37], v[192:199], v[120:123], v191, v191 op_sel_hi:[0,0,0]
	v_mfma_scale_f32_16x16x128_f8f6f4 v[124:127], v[38:45], v[192:199], v[124:127], v191, v191 op_sel_hi:[0,0,0]
	v_mfma_scale_f32_16x16x128_f8f6f4 v[96:99], v[30:37], v[200:207], v[96:99], v191, v191 op_sel_hi:[0,0,0]
	v_mfma_scale_f32_16x16x128_f8f6f4 v[100:103], v[38:45], v[200:207], v[100:103], v191, v191 op_sel_hi:[0,0,0]
	v_mfma_scale_f32_16x16x128_f8f6f4 v[80:83], v[30:37], v[208:215], v[80:83], v191, v191 op_sel_hi:[0,0,0]
	v_mfma_scale_f32_16x16x128_f8f6f4 v[84:87], v[38:45], v[208:215], v[84:87], v191, v191 op_sel_hi:[0,0,0]
	s_setprio 0
	s_barrier
	s_mov_b32 m0, s9
	v_lshl_add_u64 v[18:19], v[18:19], 0, s[22:23]
	ds_read_b128 v[216:219], v29
	ds_read_b128 v[220:223], v29 offset:1024
	ds_read_b128 v[224:227], v29 offset:2048
	ds_read_b128 v[228:231], v29 offset:3072
	global_load_lds_dwordx4 v[18:19], off
	v_lshl_add_u64 v[16:17], v[16:17], 0, s[22:23]
	s_mov_b32 m0, s28
	s_nop 0
	global_load_lds_dwordx4 v[16:17], off
	s_barrier
	s_waitcnt lgkmcnt(0)
	s_setprio 1
	s_waitcnt lgkmcnt(0)
	v_mfma_scale_f32_16x16x128_f8f6f4 v[160:163], v[216:223], v[46:53], v[160:163], v191, v191 op_sel_hi:[0,0,0]
	v_mfma_scale_f32_16x16x128_f8f6f4 v[164:167], v[224:231], v[46:53], v[164:167], v191, v191 op_sel_hi:[0,0,0]
	v_mfma_scale_f32_16x16x128_f8f6f4 v[144:147], v[216:223], v[192:199], v[144:147], v191, v191 op_sel_hi:[0,0,0]
	v_mfma_scale_f32_16x16x128_f8f6f4 v[152:155], v[224:231], v[192:199], v[152:155], v191, v191 op_sel_hi:[0,0,0]
	v_mfma_scale_f32_16x16x128_f8f6f4 v[128:131], v[216:223], v[200:207], v[128:131], v191, v191 op_sel_hi:[0,0,0]
	v_mfma_scale_f32_16x16x128_f8f6f4 v[132:135], v[224:231], v[200:207], v[132:135], v191, v191 op_sel_hi:[0,0,0]
	v_mfma_scale_f32_16x16x128_f8f6f4 v[104:107], v[216:223], v[208:215], v[104:107], v191, v191 op_sel_hi:[0,0,0]
	v_mfma_scale_f32_16x16x128_f8f6f4 v[112:115], v[224:231], v[208:215], v[112:115], v191, v191 op_sel_hi:[0,0,0]
	s_setprio 0
	s_mov_b32 m0, s66
	v_lshl_add_u64 v[16:17], v[26:27], 0, s[22:23]
	s_barrier
	ds_read_b128 v[46:49], v190 offset:49152
	ds_read_b128 v[50:53], v190 offset:50176
	ds_read_b128 v[192:195], v190 offset:51200
	ds_read_b128 v[196:199], v190 offset:52224
	ds_read_b128 v[200:203], v190 offset:53248
	ds_read_b128 v[204:207], v190 offset:54272
	ds_read_b128 v[208:211], v190 offset:55296
	ds_read_b128 v[212:215], v190 offset:56320
	global_load_lds_dwordx4 v[16:17], off
	v_lshl_add_u64 v[16:17], v[22:23], 0, s[22:23]
	s_mov_b32 m0, s67
	s_nop 0
	global_load_lds_dwordx4 v[16:17], off
	s_barrier
	s_waitcnt lgkmcnt(0)
	s_setprio 1
	s_waitcnt lgkmcnt(0)
	v_mfma_scale_f32_16x16x128_f8f6f4 v[108:111], v[30:37], v[46:53], v[108:111], v191, v191 op_sel_hi:[0,0,0]
	v_mfma_scale_f32_16x16x128_f8f6f4 v[116:119], v[38:45], v[46:53], v[116:119], v191, v191 op_sel_hi:[0,0,0]
	v_mfma_scale_f32_16x16x128_f8f6f4 v[88:91], v[30:37], v[192:199], v[88:91], v191, v191 op_sel_hi:[0,0,0]
	v_mfma_scale_f32_16x16x128_f8f6f4 v[92:95], v[38:45], v[192:199], v[92:95], v191, v191 op_sel_hi:[0,0,0]
	v_mfma_scale_f32_16x16x128_f8f6f4 v[72:75], v[30:37], v[200:207], v[72:75], v191, v191 op_sel_hi:[0,0,0]
	v_mfma_scale_f32_16x16x128_f8f6f4 v[76:79], v[38:45], v[200:207], v[76:79], v191, v191 op_sel_hi:[0,0,0]
	v_mfma_scale_f32_16x16x128_f8f6f4 v[68:71], v[30:37], v[208:215], v[68:71], v191, v191 op_sel_hi:[0,0,0]
	v_mfma_scale_f32_16x16x128_f8f6f4 v[64:67], v[38:45], v[208:215], v[64:67], v191, v191 op_sel_hi:[0,0,0]
	s_setprio 0
	s_barrier
	s_mov_b32 m0, s29
	v_lshl_add_u64 v[16:17], v[24:25], 0, s[22:23]
	global_load_lds_dwordx4 v[16:17], off
	v_lshl_add_u64 v[16:17], v[20:21], 0, s[22:23]
	s_mov_b32 m0, s52
	s_nop 0
	global_load_lds_dwordx4 v[16:17], off
	s_waitcnt vmcnt(6)
	s_barrier
	s_setprio 1
	v_mfma_scale_f32_16x16x128_f8f6f4 v[148:151], v[216:223], v[46:53], v[148:151], v191, v191 op_sel_hi:[0,0,0]
	v_mfma_scale_f32_16x16x128_f8f6f4 v[156:159], v[224:231], v[46:53], v[156:159], v191, v191 op_sel_hi:[0,0,0]
	v_mfma_scale_f32_16x16x128_f8f6f4 v[56:59], v[216:223], v[192:199], v[56:59], v191, v191 op_sel_hi:[0,0,0]
	v_mfma_scale_f32_16x16x128_f8f6f4 v[60:63], v[224:231], v[192:199], v[60:63], v191, v191 op_sel_hi:[0,0,0]
	v_mfma_scale_f32_16x16x128_f8f6f4 v[8:11], v[216:223], v[200:207], v[8:11], v191, v191 op_sel_hi:[0,0,0]
	v_mfma_scale_f32_16x16x128_f8f6f4 v[12:15], v[224:231], v[200:207], v[12:15], v191, v191 op_sel_hi:[0,0,0]
	v_mfma_scale_f32_16x16x128_f8f6f4 v[4:7], v[216:223], v[208:215], v[4:7], v191, v191 op_sel_hi:[0,0,0]
	v_mfma_scale_f32_16x16x128_f8f6f4 v[0:3], v[224:231], v[208:215], v[0:3], v191, v191 op_sel_hi:[0,0,0]
	s_setprio 0
	s_add_u32 s50, s50, 0x100
	s_addc_u32 s51, s51, 0
	s_add_i32 s6, s53, 2
	s_add_u32 s48, s48, 0x100
	s_addc_u32 s49, s49, 0
	s_cmp_ge_i32 s53, s64
	s_mov_b32 s53, s6
	s_barrier
	s_cbranch_scc0 .LBB0_2762
